# cross-attention K chunks: MFMA body waited for the next chunk's staging loads (vmcnt too strict on 3 of 4 chunks); counted waits vmcnt(11..8) with 8 one-dword loads on the last chunk to keep the count
# speedup vs baseline: 1.0138x; 1.0012x over previous
; #define MFMA16(b, a, c) __builtin_amdgcn_mfma_f32_16x16x32_bf16((b), (a), (c), 0, 0, 0)
; __device__ __forceinline__ void xattn_unit(LAS unsigned char* lds, int hd, int qt, const bf16_t* QX, const bf16_t* KX, const bf16_t* VX, bf16_t* O) {
;     ...
;     for (int kc = 0; kc < 4; ++kc) {
;         __syncthreads();
;         stage_store<NMEM, 128, 8>(X, pf, tid);
;         bf16x8 aq[4];
; #pragma unroll
;         for (int ks = 0; ks < 4; ++ks) aq[ks] = *(const bf16x8*)(QX + trow * D + hd * XD + kc * 128 + 32 * ks + 8 * fq);
;         if (kc < 3) stage_load<NMEM, 128>(pf, KX + hd * XD + (kc + 1) * 128, D, tid);
;         __syncthreads();
; #pragma unroll
;         for (int ks = 0; ks < 4; ++ks)
; #pragma unroll
;             for (int j = 0; j < 16; ++j) S[j] = MFMA16(row_frag(X, (128 + 8) * 2, 16 * j, 32 * ks, lane), aq[ks], S[j]);
.LBB0_979:
	s_waitcnt lgkmcnt(0)
	s_barrier
	ds_read_b128 v[210:213], v200
	ds_read_b128 v[214:217], v200 offset:4352
	s_waitcnt vmcnt(11) lgkmcnt(1)
	v_mfma_f32_16x16x32_bf16 v[94:97], v[210:213], v[110:113], v[94:97]
	ds_read_b128 v[210:213], v200 offset:8704
	s_add_u32 s10, s10, 0x100
	s_addc_u32 s11, s11, 0
	s_waitcnt lgkmcnt(1)
	v_mfma_f32_16x16x32_bf16 v[90:93], v[214:217], v[110:113], v[90:93]
	ds_read_b128 v[214:217], v200 offset:13056
	s_cmpk_lg_i32 s10, 0x400
	s_waitcnt lgkmcnt(1)
	v_mfma_f32_16x16x32_bf16 v[86:89], v[210:213], v[110:113], v[86:89]
	ds_read_b128 v[210:213], v200 offset:17408
	s_waitcnt lgkmcnt(1)
	v_mfma_f32_16x16x32_bf16 v[82:85], v[214:217], v[110:113], v[82:85]
	ds_read_b128 v[214:217], v200 offset:21760
	s_waitcnt lgkmcnt(1)
	v_mfma_f32_16x16x32_bf16 v[78:81], v[210:213], v[110:113], v[78:81]
	ds_read_b128 v[210:213], v200 offset:26112
	s_waitcnt lgkmcnt(1)
	v_mfma_f32_16x16x32_bf16 v[74:77], v[214:217], v[110:113], v[74:77]
	ds_read_b128 v[214:217], v200 offset:30464
	s_waitcnt lgkmcnt(1)
	v_mfma_f32_16x16x32_bf16 v[70:73], v[210:213], v[110:113], v[70:73]
	ds_read_b128 v[210:213], v200 offset:34816
	s_waitcnt lgkmcnt(1)
	v_mfma_f32_16x16x32_bf16 v[66:69], v[214:217], v[110:113], v[66:69]
	ds_read_b128 v[214:217], v200 offset:39168
	s_waitcnt lgkmcnt(1)
	v_mfma_f32_16x16x32_bf16 v[62:65], v[210:213], v[110:113], v[62:65]
	ds_read_b128 v[210:213], v200 offset:43520
	s_waitcnt lgkmcnt(1)
	v_mfma_f32_16x16x32_bf16 v[58:61], v[214:217], v[110:113], v[58:61]
	ds_read_b128 v[214:217], v200 offset:47872
	s_waitcnt lgkmcnt(1)
	v_mfma_f32_16x16x32_bf16 v[54:57], v[210:213], v[110:113], v[54:57]
	ds_read_b128 v[210:213], v200 offset:52224
	s_waitcnt lgkmcnt(1)
	v_mfma_f32_16x16x32_bf16 v[50:53], v[214:217], v[110:113], v[50:53]
	ds_read_b128 v[214:217], v200 offset:56576
	s_waitcnt lgkmcnt(1)
	v_mfma_f32_16x16x32_bf16 v[46:49], v[210:213], v[110:113], v[46:49]
	ds_read_b128 v[210:213], v200 offset:60928
	s_waitcnt lgkmcnt(1)
	v_mfma_f32_16x16x32_bf16 v[42:45], v[214:217], v[110:113], v[42:45]
	ds_read_b128 v[214:217], v200 offset:65280
	s_waitcnt lgkmcnt(1)
	v_mfma_f32_16x16x32_bf16 v[38:41], v[210:213], v[110:113], v[38:41]
	ds_read_b128 v[210:213], v200 offset:64
	s_waitcnt lgkmcnt(1)
	v_mfma_f32_16x16x32_bf16 v[34:37], v[214:217], v[110:113], v[34:37]
	ds_read_b128 v[110:113], v200 offset:4416
	s_waitcnt vmcnt(10) lgkmcnt(0)
	v_mfma_f32_16x16x32_bf16 v[90:93], v[110:113], v[106:109], v[90:93]
	ds_read_b128 v[110:113], v200 offset:13120
	s_waitcnt lgkmcnt(0)
	v_mfma_f32_16x16x32_bf16 v[82:85], v[110:113], v[106:109], v[82:85]
	ds_read_b128 v[110:113], v200 offset:21824
	s_waitcnt lgkmcnt(0)
	v_mfma_f32_16x16x32_bf16 v[74:77], v[110:113], v[106:109], v[74:77]
	ds_read_b128 v[110:113], v200 offset:30528
	s_waitcnt lgkmcnt(0)
	v_mfma_f32_16x16x32_bf16 v[66:69], v[110:113], v[106:109], v[66:69]
	ds_read_b128 v[110:113], v200 offset:39232
	v_mfma_f32_16x16x32_bf16 v[94:97], v[210:213], v[106:109], v[94:97]
	ds_read_b128 v[210:213], v200 offset:8768
	s_waitcnt lgkmcnt(1)
	v_mfma_f32_16x16x32_bf16 v[58:61], v[110:113], v[106:109], v[58:61]
	ds_read_b128 v[110:113], v200 offset:47936
	s_waitcnt lgkmcnt(1)
	v_mfma_f32_16x16x32_bf16 v[86:89], v[210:213], v[106:109], v[86:89]
	ds_read_b128 v[210:213], v200 offset:17472
	s_waitcnt lgkmcnt(1)
	v_mfma_f32_16x16x32_bf16 v[50:53], v[110:113], v[106:109], v[50:53]
	ds_read_b128 v[110:113], v200 offset:56640
	s_waitcnt lgkmcnt(1)
	v_mfma_f32_16x16x32_bf16 v[78:81], v[210:213], v[106:109], v[78:81]
	ds_read_b128 v[210:213], v200 offset:26176
	s_waitcnt lgkmcnt(1)
	v_mfma_f32_16x16x32_bf16 v[42:45], v[110:113], v[106:109], v[42:45]
	ds_read_b128 v[110:113], v200 offset:65344
	s_waitcnt lgkmcnt(0)
	v_mfma_f32_16x16x32_bf16 v[34:37], v[110:113], v[106:109], v[34:37]
	ds_read_b128 v[110:113], v200 offset:8832
	s_waitcnt vmcnt(9) lgkmcnt(0)
	v_mfma_f32_16x16x32_bf16 v[86:89], v[110:113], v[102:105], v[86:89]
	ds_read_b128 v[110:113], v200 offset:17536
	v_mfma_f32_16x16x32_bf16 v[70:73], v[210:213], v[106:109], v[70:73]
	ds_read_b128 v[210:213], v200 offset:34880
	s_waitcnt lgkmcnt(1)
	v_mfma_f32_16x16x32_bf16 v[78:81], v[110:113], v[102:105], v[78:81]
	ds_read_b128 v[110:113], v200 offset:26240
	s_waitcnt lgkmcnt(0)
; #define MFMA16(b, a, c) __builtin_amdgcn_mfma_f32_16x16x32_bf16((b), (a), (c), 0, 0, 0)
; __device__ __forceinline__ void xattn_unit(LAS unsigned char* lds, int hd, int qt, const bf16_t* QX, const bf16_t* KX, const bf16_t* VX, bf16_t* O) {
;     ...
; #pragma unroll
;         for (int ks = 0; ks < 4; ++ks)
; #pragma unroll
;             for (int j = 0; j < 16; ++j) S[j] = MFMA16(row_frag(X, (128 + 8) * 2, 16 * j, 32 * ks, lane), aq[ks], S[j]);
	v_mfma_f32_16x16x32_bf16 v[70:73], v[110:113], v[102:105], v[70:73]
	ds_read_b128 v[110:113], v200 offset:34944
	v_mfma_f32_16x16x32_bf16 v[62:65], v[210:213], v[106:109], v[62:65]
	ds_read_b128 v[210:213], v200 offset:43584
	s_waitcnt lgkmcnt(0)
	v_mfma_f32_16x16x32_bf16 v[54:57], v[210:213], v[106:109], v[54:57]
	ds_read_b128 v[210:213], v200 offset:52288
	s_waitcnt lgkmcnt(0)
	v_mfma_f32_16x16x32_bf16 v[46:49], v[210:213], v[106:109], v[46:49]
	ds_read_b128 v[210:213], v200 offset:60992
	s_waitcnt lgkmcnt(0)
	v_mfma_f32_16x16x32_bf16 v[38:41], v[210:213], v[106:109], v[38:41]
	ds_read_b128 v[106:109], v200 offset:4480
	ds_read_b128 v[210:213], v200 offset:128
	s_waitcnt lgkmcnt(1)
	v_mfma_f32_16x16x32_bf16 v[90:93], v[106:109], v[102:105], v[90:93]
	ds_read_b128 v[106:109], v200 offset:13184
	s_waitcnt lgkmcnt(0)
	v_mfma_f32_16x16x32_bf16 v[82:85], v[106:109], v[102:105], v[82:85]
	ds_read_b128 v[106:109], v200 offset:21888
	s_waitcnt lgkmcnt(0)
	v_mfma_f32_16x16x32_bf16 v[74:77], v[106:109], v[102:105], v[74:77]
	ds_read_b128 v[106:109], v200 offset:30592
	s_waitcnt lgkmcnt(0)
	v_mfma_f32_16x16x32_bf16 v[66:69], v[106:109], v[102:105], v[66:69]
	ds_read_b128 v[106:109], v200 offset:39296
	v_mfma_f32_16x16x32_bf16 v[62:65], v[110:113], v[102:105], v[62:65]
	ds_read_b128 v[110:113], v200 offset:43648
	s_waitcnt lgkmcnt(1)
	v_mfma_f32_16x16x32_bf16 v[58:61], v[106:109], v[102:105], v[58:61]
	ds_read_b128 v[106:109], v200 offset:48000
	s_waitcnt lgkmcnt(1)
	v_mfma_f32_16x16x32_bf16 v[54:57], v[110:113], v[102:105], v[54:57]
	ds_read_b128 v[110:113], v200 offset:52352
	s_waitcnt lgkmcnt(1)
	v_mfma_f32_16x16x32_bf16 v[50:53], v[106:109], v[102:105], v[50:53]
	ds_read_b128 v[106:109], v200 offset:56704
	s_waitcnt lgkmcnt(1)
	v_mfma_f32_16x16x32_bf16 v[46:49], v[110:113], v[102:105], v[46:49]
	ds_read_b128 v[110:113], v200 offset:61056
	s_waitcnt lgkmcnt(1)
	v_mfma_f32_16x16x32_bf16 v[42:45], v[106:109], v[102:105], v[42:45]
	ds_read_b128 v[106:109], v200 offset:65408
	v_mfma_f32_16x16x32_bf16 v[94:97], v[210:213], v[102:105], v[94:97]
	s_waitcnt lgkmcnt(1)
	v_mfma_f32_16x16x32_bf16 v[38:41], v[110:113], v[102:105], v[38:41]
	ds_read_b128 v[110:113], v200 offset:192
	s_waitcnt lgkmcnt(1)
	v_mfma_f32_16x16x32_bf16 v[34:37], v[106:109], v[102:105], v[34:37]
	ds_read_b128 v[102:105], v200 offset:4544
	ds_read_b128 v[106:109], v200 offset:8896
	s_waitcnt vmcnt(8) lgkmcnt(1)
	v_mfma_f32_16x16x32_bf16 v[90:93], v[102:105], v[98:101], v[90:93]
	ds_read_b128 v[102:105], v200 offset:13248
	s_waitcnt lgkmcnt(1)
	v_mfma_f32_16x16x32_bf16 v[86:89], v[106:109], v[98:101], v[86:89]
	ds_read_b128 v[106:109], v200 offset:17600
	s_waitcnt lgkmcnt(1)
	v_mfma_f32_16x16x32_bf16 v[82:85], v[102:105], v[98:101], v[82:85]
	ds_read_b128 v[102:105], v200 offset:21952
	s_waitcnt lgkmcnt(1)
	v_mfma_f32_16x16x32_bf16 v[78:81], v[106:109], v[98:101], v[78:81]
	ds_read_b128 v[106:109], v200 offset:26304
	s_waitcnt lgkmcnt(1)
	v_mfma_f32_16x16x32_bf16 v[74:77], v[102:105], v[98:101], v[74:77]
	ds_read_b128 v[102:105], v200 offset:30656
	s_waitcnt lgkmcnt(1)
	v_mfma_f32_16x16x32_bf16 v[70:73], v[106:109], v[98:101], v[70:73]
	ds_read_b128 v[106:109], v200 offset:35008
	s_waitcnt lgkmcnt(1)
	v_mfma_f32_16x16x32_bf16 v[66:69], v[102:105], v[98:101], v[66:69]
	ds_read_b128 v[102:105], v200 offset:39360
	s_waitcnt lgkmcnt(1)
	v_mfma_f32_16x16x32_bf16 v[62:65], v[106:109], v[98:101], v[62:65]
	ds_read_b128 v[106:109], v200 offset:43712
	s_waitcnt lgkmcnt(1)
	v_mfma_f32_16x16x32_bf16 v[58:61], v[102:105], v[98:101], v[58:61]
	ds_read_b128 v[102:105], v200 offset:48064
	s_waitcnt lgkmcnt(1)
	v_mfma_f32_16x16x32_bf16 v[54:57], v[106:109], v[98:101], v[54:57]
	ds_read_b128 v[106:109], v200 offset:52416
	s_waitcnt lgkmcnt(1)
	v_mfma_f32_16x16x32_bf16 v[50:53], v[102:105], v[98:101], v[50:53]
	ds_read_b128 v[102:105], v200 offset:56768
	s_waitcnt lgkmcnt(1)
	v_mfma_f32_16x16x32_bf16 v[46:49], v[106:109], v[98:101], v[46:49]
	ds_read_b128 v[106:109], v200 offset:61120
	s_waitcnt lgkmcnt(1)
	v_mfma_f32_16x16x32_bf16 v[42:45], v[102:105], v[98:101], v[42:45]
	ds_read_b128 v[102:105], v200 offset:65472
	v_mfma_f32_16x16x32_bf16 v[94:97], v[110:113], v[98:101], v[94:97]
	s_waitcnt lgkmcnt(1)
	v_mfma_f32_16x16x32_bf16 v[38:41], v[106:109], v[98:101], v[38:41]
	s_waitcnt lgkmcnt(0)
	v_mfma_f32_16x16x32_bf16 v[34:37], v[102:105], v[98:101], v[34:37]
	s_cbranch_scc0 .LBB0_982

; __device__ __forceinline__ void xattn_unit(LAS unsigned char* lds, int hd, int qt, const bf16_t* QX, const bf16_t* KX, const bf16_t* VX, bf16_t* O) {
;     ...
;         for (int ks = 0; ks < 4; ++ks) aq[ks] = *(const bf16x8*)(QX + trow * D + hd * XD + kc * 128 + 32 * ks + 8 * fq);
;         if (kc < 3) stage_load<NMEM, 128>(pf, KX + hd * XD + (kc + 1) * 128, D, tid);
.Lxa_last_0:
	global_load_dword v228, v[180:181], off
	global_load_dword v229, v[180:181], off
	global_load_dword v230, v[180:181], off
	global_load_dword v231, v[180:181], off
	global_load_dword v232, v[180:181], off
	global_load_dword v233, v[180:181], off
	global_load_dword v234, v[180:181], off
	global_load_dword v235, v[180:181], off
	s_branch .LBB0_979

; #define MFMA16(b, a, c) __builtin_amdgcn_mfma_f32_16x16x32_bf16((b), (a), (c), 0, 0, 0)
; __device__ __forceinline__ void xattn_unit(LAS unsigned char* lds, int hd, int qt, const bf16_t* QX, const bf16_t* KX, const bf16_t* VX, bf16_t* O) {
;     ...
;     for (int kc = 0; kc < 4; ++kc) {
;         __syncthreads();
;         stage_store<NMEM, 128, 8>(X, pf, tid);
;         bf16x8 aq[4];
; #pragma unroll
;         for (int ks = 0; ks < 4; ++ks) aq[ks] = *(const bf16x8*)(QX + trow * D + hd * XD + kc * 128 + 32 * ks + 8 * fq);
;         if (kc < 3) stage_load<NMEM, 128>(pf, KX + hd * XD + (kc + 1) * 128, D, tid);
;         __syncthreads();
; #pragma unroll
;         for (int ks = 0; ks < 4; ++ks)
; #pragma unroll
;             for (int j = 0; j < 16; ++j) S[j] = MFMA16(row_frag(X, (128 + 8) * 2, 16 * j, 32 * ks, lane), aq[ks], S[j]);
.LBB0_1814:
	s_waitcnt lgkmcnt(0)
	s_barrier
	ds_read_b128 v[210:213], v200
	ds_read_b128 v[214:217], v200 offset:4352
	s_waitcnt vmcnt(11) lgkmcnt(1)
	v_mfma_f32_16x16x32_bf16 v[94:97], v[210:213], v[110:113], v[94:97]
	ds_read_b128 v[210:213], v200 offset:8704
	s_add_u32 s12, s12, 0x100
	s_addc_u32 s13, s13, 0
	s_waitcnt lgkmcnt(1)
	v_mfma_f32_16x16x32_bf16 v[90:93], v[214:217], v[110:113], v[90:93]
	ds_read_b128 v[214:217], v200 offset:13056
	s_cmpk_lg_i32 s12, 0x400
	s_waitcnt lgkmcnt(1)
	v_mfma_f32_16x16x32_bf16 v[86:89], v[210:213], v[110:113], v[86:89]
	ds_read_b128 v[210:213], v200 offset:17408
	s_waitcnt lgkmcnt(1)
	v_mfma_f32_16x16x32_bf16 v[82:85], v[214:217], v[110:113], v[82:85]
	ds_read_b128 v[214:217], v200 offset:21760
	s_waitcnt lgkmcnt(1)
	v_mfma_f32_16x16x32_bf16 v[78:81], v[210:213], v[110:113], v[78:81]
	ds_read_b128 v[210:213], v200 offset:26112
	s_waitcnt lgkmcnt(1)
	v_mfma_f32_16x16x32_bf16 v[74:77], v[214:217], v[110:113], v[74:77]
	ds_read_b128 v[214:217], v200 offset:30464
	s_waitcnt lgkmcnt(1)
	v_mfma_f32_16x16x32_bf16 v[70:73], v[210:213], v[110:113], v[70:73]
	ds_read_b128 v[210:213], v200 offset:34816
	s_waitcnt lgkmcnt(1)
	v_mfma_f32_16x16x32_bf16 v[66:69], v[214:217], v[110:113], v[66:69]
	ds_read_b128 v[214:217], v200 offset:39168
	s_waitcnt lgkmcnt(1)
	v_mfma_f32_16x16x32_bf16 v[62:65], v[210:213], v[110:113], v[62:65]
	ds_read_b128 v[210:213], v200 offset:43520
	s_waitcnt lgkmcnt(1)
	v_mfma_f32_16x16x32_bf16 v[58:61], v[214:217], v[110:113], v[58:61]
	ds_read_b128 v[214:217], v200 offset:47872
	s_waitcnt lgkmcnt(1)
	v_mfma_f32_16x16x32_bf16 v[54:57], v[210:213], v[110:113], v[54:57]
	ds_read_b128 v[210:213], v200 offset:52224
	s_waitcnt lgkmcnt(1)
	v_mfma_f32_16x16x32_bf16 v[50:53], v[214:217], v[110:113], v[50:53]
	ds_read_b128 v[214:217], v200 offset:56576
	s_waitcnt lgkmcnt(1)
	v_mfma_f32_16x16x32_bf16 v[46:49], v[210:213], v[110:113], v[46:49]
	ds_read_b128 v[210:213], v200 offset:60928
	s_waitcnt lgkmcnt(1)
	v_mfma_f32_16x16x32_bf16 v[42:45], v[214:217], v[110:113], v[42:45]
	ds_read_b128 v[214:217], v200 offset:65280
	s_waitcnt lgkmcnt(1)
	v_mfma_f32_16x16x32_bf16 v[38:41], v[210:213], v[110:113], v[38:41]
	ds_read_b128 v[210:213], v200 offset:64
	s_waitcnt lgkmcnt(1)
	v_mfma_f32_16x16x32_bf16 v[34:37], v[214:217], v[110:113], v[34:37]
	ds_read_b128 v[110:113], v200 offset:4416
	s_waitcnt vmcnt(10) lgkmcnt(0)
	v_mfma_f32_16x16x32_bf16 v[90:93], v[110:113], v[106:109], v[90:93]
	ds_read_b128 v[110:113], v200 offset:13120
	s_waitcnt lgkmcnt(0)
	v_mfma_f32_16x16x32_bf16 v[82:85], v[110:113], v[106:109], v[82:85]
	ds_read_b128 v[110:113], v200 offset:21824
	s_waitcnt lgkmcnt(0)
	v_mfma_f32_16x16x32_bf16 v[74:77], v[110:113], v[106:109], v[74:77]
	ds_read_b128 v[110:113], v200 offset:30528
	s_waitcnt lgkmcnt(0)
	v_mfma_f32_16x16x32_bf16 v[66:69], v[110:113], v[106:109], v[66:69]
	ds_read_b128 v[110:113], v200 offset:39232
	v_mfma_f32_16x16x32_bf16 v[94:97], v[210:213], v[106:109], v[94:97]
	ds_read_b128 v[210:213], v200 offset:8768
	s_waitcnt lgkmcnt(1)
	v_mfma_f32_16x16x32_bf16 v[58:61], v[110:113], v[106:109], v[58:61]
	ds_read_b128 v[110:113], v200 offset:47936
	s_waitcnt lgkmcnt(1)
	v_mfma_f32_16x16x32_bf16 v[86:89], v[210:213], v[106:109], v[86:89]
	ds_read_b128 v[210:213], v200 offset:17472
	s_waitcnt lgkmcnt(1)
	v_mfma_f32_16x16x32_bf16 v[50:53], v[110:113], v[106:109], v[50:53]
	ds_read_b128 v[110:113], v200 offset:56640
	s_waitcnt lgkmcnt(1)
	v_mfma_f32_16x16x32_bf16 v[78:81], v[210:213], v[106:109], v[78:81]
	ds_read_b128 v[210:213], v200 offset:26176
	s_waitcnt lgkmcnt(1)
	v_mfma_f32_16x16x32_bf16 v[42:45], v[110:113], v[106:109], v[42:45]
	ds_read_b128 v[110:113], v200 offset:65344
	s_waitcnt lgkmcnt(0)
	v_mfma_f32_16x16x32_bf16 v[34:37], v[110:113], v[106:109], v[34:37]
	ds_read_b128 v[110:113], v200 offset:8832
	s_waitcnt vmcnt(9) lgkmcnt(0)
	v_mfma_f32_16x16x32_bf16 v[86:89], v[110:113], v[102:105], v[86:89]
	ds_read_b128 v[110:113], v200 offset:17536
	v_mfma_f32_16x16x32_bf16 v[70:73], v[210:213], v[106:109], v[70:73]
	ds_read_b128 v[210:213], v200 offset:34880
	s_waitcnt lgkmcnt(1)
	v_mfma_f32_16x16x32_bf16 v[78:81], v[110:113], v[102:105], v[78:81]
	ds_read_b128 v[110:113], v200 offset:26240
	s_waitcnt lgkmcnt(0)
; #define MFMA16(b, a, c) __builtin_amdgcn_mfma_f32_16x16x32_bf16((b), (a), (c), 0, 0, 0)
; __device__ __forceinline__ void xattn_unit(LAS unsigned char* lds, int hd, int qt, const bf16_t* QX, const bf16_t* KX, const bf16_t* VX, bf16_t* O) {
;     ...
; #pragma unroll
;         for (int ks = 0; ks < 4; ++ks)
; #pragma unroll
;             for (int j = 0; j < 16; ++j) S[j] = MFMA16(row_frag(X, (128 + 8) * 2, 16 * j, 32 * ks, lane), aq[ks], S[j]);
	v_mfma_f32_16x16x32_bf16 v[70:73], v[110:113], v[102:105], v[70:73]
	ds_read_b128 v[110:113], v200 offset:34944
	v_mfma_f32_16x16x32_bf16 v[62:65], v[210:213], v[106:109], v[62:65]
	ds_read_b128 v[210:213], v200 offset:43584
	s_waitcnt lgkmcnt(0)
	v_mfma_f32_16x16x32_bf16 v[54:57], v[210:213], v[106:109], v[54:57]
	ds_read_b128 v[210:213], v200 offset:52288
	s_waitcnt lgkmcnt(0)
	v_mfma_f32_16x16x32_bf16 v[46:49], v[210:213], v[106:109], v[46:49]
	ds_read_b128 v[210:213], v200 offset:60992
	s_waitcnt lgkmcnt(0)
	v_mfma_f32_16x16x32_bf16 v[38:41], v[210:213], v[106:109], v[38:41]
	ds_read_b128 v[106:109], v200 offset:4480
	ds_read_b128 v[210:213], v200 offset:128
	s_waitcnt lgkmcnt(1)
	v_mfma_f32_16x16x32_bf16 v[90:93], v[106:109], v[102:105], v[90:93]
	ds_read_b128 v[106:109], v200 offset:13184
	s_waitcnt lgkmcnt(0)
	v_mfma_f32_16x16x32_bf16 v[82:85], v[106:109], v[102:105], v[82:85]
	ds_read_b128 v[106:109], v200 offset:21888
	s_waitcnt lgkmcnt(0)
	v_mfma_f32_16x16x32_bf16 v[74:77], v[106:109], v[102:105], v[74:77]
	ds_read_b128 v[106:109], v200 offset:30592
	s_waitcnt lgkmcnt(0)
	v_mfma_f32_16x16x32_bf16 v[66:69], v[106:109], v[102:105], v[66:69]
	ds_read_b128 v[106:109], v200 offset:39296
	v_mfma_f32_16x16x32_bf16 v[62:65], v[110:113], v[102:105], v[62:65]
	ds_read_b128 v[110:113], v200 offset:43648
	s_waitcnt lgkmcnt(1)
	v_mfma_f32_16x16x32_bf16 v[58:61], v[106:109], v[102:105], v[58:61]
	ds_read_b128 v[106:109], v200 offset:48000
	s_waitcnt lgkmcnt(1)
	v_mfma_f32_16x16x32_bf16 v[54:57], v[110:113], v[102:105], v[54:57]
	ds_read_b128 v[110:113], v200 offset:52352
	s_waitcnt lgkmcnt(1)
	v_mfma_f32_16x16x32_bf16 v[50:53], v[106:109], v[102:105], v[50:53]
	ds_read_b128 v[106:109], v200 offset:56704
	s_waitcnt lgkmcnt(1)
	v_mfma_f32_16x16x32_bf16 v[46:49], v[110:113], v[102:105], v[46:49]
	ds_read_b128 v[110:113], v200 offset:61056
	s_waitcnt lgkmcnt(1)
	v_mfma_f32_16x16x32_bf16 v[42:45], v[106:109], v[102:105], v[42:45]
	ds_read_b128 v[106:109], v200 offset:65408
	v_mfma_f32_16x16x32_bf16 v[94:97], v[210:213], v[102:105], v[94:97]
	s_waitcnt lgkmcnt(1)
	v_mfma_f32_16x16x32_bf16 v[38:41], v[110:113], v[102:105], v[38:41]
	ds_read_b128 v[110:113], v200 offset:192
	s_waitcnt lgkmcnt(1)
	v_mfma_f32_16x16x32_bf16 v[34:37], v[106:109], v[102:105], v[34:37]
	ds_read_b128 v[102:105], v200 offset:4544
	ds_read_b128 v[106:109], v200 offset:8896
	s_waitcnt vmcnt(8) lgkmcnt(1)
	v_mfma_f32_16x16x32_bf16 v[90:93], v[102:105], v[98:101], v[90:93]
	ds_read_b128 v[102:105], v200 offset:13248
	s_waitcnt lgkmcnt(1)
	v_mfma_f32_16x16x32_bf16 v[86:89], v[106:109], v[98:101], v[86:89]
	ds_read_b128 v[106:109], v200 offset:17600
	s_waitcnt lgkmcnt(1)
	v_mfma_f32_16x16x32_bf16 v[82:85], v[102:105], v[98:101], v[82:85]
	ds_read_b128 v[102:105], v200 offset:21952
	s_waitcnt lgkmcnt(1)
	v_mfma_f32_16x16x32_bf16 v[78:81], v[106:109], v[98:101], v[78:81]
	ds_read_b128 v[106:109], v200 offset:26304
	s_waitcnt lgkmcnt(1)
	v_mfma_f32_16x16x32_bf16 v[74:77], v[102:105], v[98:101], v[74:77]
	ds_read_b128 v[102:105], v200 offset:30656
	s_waitcnt lgkmcnt(1)
	v_mfma_f32_16x16x32_bf16 v[70:73], v[106:109], v[98:101], v[70:73]
	ds_read_b128 v[106:109], v200 offset:35008
	s_waitcnt lgkmcnt(1)
	v_mfma_f32_16x16x32_bf16 v[66:69], v[102:105], v[98:101], v[66:69]
	ds_read_b128 v[102:105], v200 offset:39360
	s_waitcnt lgkmcnt(1)
	v_mfma_f32_16x16x32_bf16 v[62:65], v[106:109], v[98:101], v[62:65]
	ds_read_b128 v[106:109], v200 offset:43712
	s_waitcnt lgkmcnt(1)
	v_mfma_f32_16x16x32_bf16 v[58:61], v[102:105], v[98:101], v[58:61]
	ds_read_b128 v[102:105], v200 offset:48064
	s_waitcnt lgkmcnt(1)
	v_mfma_f32_16x16x32_bf16 v[54:57], v[106:109], v[98:101], v[54:57]
	ds_read_b128 v[106:109], v200 offset:52416
	s_waitcnt lgkmcnt(1)
	v_mfma_f32_16x16x32_bf16 v[50:53], v[102:105], v[98:101], v[50:53]
	ds_read_b128 v[102:105], v200 offset:56768
	s_waitcnt lgkmcnt(1)
	v_mfma_f32_16x16x32_bf16 v[46:49], v[106:109], v[98:101], v[46:49]
	ds_read_b128 v[106:109], v200 offset:61120
	s_waitcnt lgkmcnt(1)
	v_mfma_f32_16x16x32_bf16 v[42:45], v[102:105], v[98:101], v[42:45]
	ds_read_b128 v[102:105], v200 offset:65472
	v_mfma_f32_16x16x32_bf16 v[94:97], v[110:113], v[98:101], v[94:97]
	s_waitcnt lgkmcnt(1)
	v_mfma_f32_16x16x32_bf16 v[38:41], v[106:109], v[98:101], v[38:41]
	s_waitcnt lgkmcnt(0)
	v_mfma_f32_16x16x32_bf16 v[34:37], v[102:105], v[98:101], v[34:37]
	s_cbranch_scc0 .LBB0_1817
